# scan R2: prefetch all LDS operands one chunk ahead, S0 stores transposed through LDS into full-line dwordx4 stores
# speedup vs baseline: 1.0349x; 1.0349x over previous
.LBB0_1920:
	s_and_b64 vcc, exec, s[0:1]
	s_cbranch_vccz .LBB0_1927
	v_readlane_b32 s22, v253, 0
	v_readlane_b32 s23, v253, 1
	s_mov_b32 s23, 0
	v_mov_b32_e32 v1, v0
	s_lshl_b64 s[0:1], s[22:23], 7
	s_add_u32 s4, s48, 0x10800000
	s_waitcnt vmcnt(0)
	v_add_u32_e32 v74, 0x1400, v1
	v_ashrrev_i32_e32 v4, 10, v1
	v_ashrrev_i32_e32 v100, 10, v74
	s_addc_u32 s5, s49, 0
	v_and_b32_e32 v2, 0x200, v1
	v_ashrrev_i32_e32 v5, 31, v4
	v_ashrrev_i32_e32 v101, 31, v100
	v_mov_b32_e32 v94, s81
	v_mov_b32_e32 v95, s5
	v_cmp_eq_u32_e32 vcc, 0, v2
	v_mov_b32_e32 v96, s80
	v_mov_b32_e32 v97, s4
	s_waitcnt lgkmcnt(0)
	v_lshl_add_u64 v[2:3], s[0:1], 0, v[4:5]
	v_lshl_add_u64 v[74:75], s[0:1], 0, v[100:101]
	v_cndmask_b32_e32 v7, v94, v95, vcc
	v_cndmask_b32_e32 v6, v96, v97, vcc
	v_lshlrev_b64 v[2:3], 13, v[2:3]
	v_lshlrev_b32_e32 v120, 4, v1
	v_lshlrev_b64 v[74:75], 13, v[74:75]
	v_lshl_add_u64 v[8:9], v[6:7], 0, v[2:3]
	v_and_b32_e32 v2, 0x1ff0, v120
	v_mov_b32_e32 v3, 0
	v_lshl_add_u64 v[74:75], v[6:7], 0, v[74:75]
	v_lshl_add_u64 v[8:9], v[8:9], 0, v[2:3]
	v_lshl_add_u64 v[74:75], v[74:75], 0, v[2:3]
	global_load_dwordx4 v[34:37], v[8:9], off
	v_add_u32_e32 v78, 0x1600, v1
	global_load_dwordx4 v[74:77], v[74:75], off
	v_add_u32_e32 v8, 0x200, v1
	v_ashrrev_i32_e32 v10, 10, v8
	v_ashrrev_i32_e32 v11, 31, v10
	v_lshl_add_u64 v[12:13], s[0:1], 0, v[10:11]
	v_cndmask_b32_e32 v9, v95, v94, vcc
	v_cndmask_b32_e32 v8, v97, v96, vcc
	v_lshlrev_b64 v[12:13], 13, v[12:13]
	v_lshl_add_u64 v[12:13], v[8:9], 0, v[12:13]
	v_lshl_add_u64 v[12:13], v[12:13], 0, v[2:3]
	global_load_dwordx4 v[38:41], v[12:13], off
	v_add_u32_e32 v12, 0x400, v1
	v_ashrrev_i32_e32 v12, 10, v12
	v_ashrrev_i32_e32 v13, 31, v12
	v_lshl_add_u64 v[14:15], s[0:1], 0, v[12:13]
	v_lshlrev_b64 v[14:15], 13, v[14:15]
	v_lshl_add_u64 v[14:15], v[6:7], 0, v[14:15]
	v_lshl_add_u64 v[14:15], v[14:15], 0, v[2:3]
	global_load_dwordx4 v[42:45], v[14:15], off
	v_add_u32_e32 v14, 0x600, v1
	v_ashrrev_i32_e32 v16, 10, v14
	v_and_b32_e32 v14, 0x200, v14
	v_ashrrev_i32_e32 v17, 31, v16
	v_cmp_eq_u32_e64 s[4:5], 0, v14
	v_lshl_add_u64 v[18:19], s[0:1], 0, v[16:17]
	v_lshlrev_b64 v[18:19], 13, v[18:19]
	v_cndmask_b32_e64 v15, v94, v95, s[4:5]
	v_cndmask_b32_e64 v14, v96, v97, s[4:5]
	v_lshl_add_u64 v[18:19], v[14:15], 0, v[18:19]
	v_lshl_add_u64 v[18:19], v[18:19], 0, v[2:3]
	global_load_dwordx4 v[46:49], v[18:19], off
	v_add_u32_e32 v18, 0x800, v1
	v_ashrrev_i32_e32 v18, 10, v18
	v_ashrrev_i32_e32 v19, 31, v18
	v_lshl_add_u64 v[20:21], s[0:1], 0, v[18:19]
	v_lshlrev_b64 v[20:21], 13, v[20:21]
	v_lshl_add_u64 v[20:21], v[6:7], 0, v[20:21]
	v_lshl_add_u64 v[20:21], v[20:21], 0, v[2:3]
	global_load_dwordx4 v[50:53], v[20:21], off
	v_add_u32_e32 v20, 0xa00, v1
	v_ashrrev_i32_e32 v22, 10, v20
	v_and_b32_e32 v20, 0x200, v20
	v_ashrrev_i32_e32 v23, 31, v22
	v_cmp_eq_u32_e64 s[6:7], 0, v20
	v_lshl_add_u64 v[24:25], s[0:1], 0, v[22:23]
	v_lshlrev_b64 v[24:25], 13, v[24:25]
	v_cndmask_b32_e64 v21, v94, v95, s[6:7]
	v_cndmask_b32_e64 v20, v96, v97, s[6:7]
	v_lshl_add_u64 v[24:25], v[20:21], 0, v[24:25]
	v_lshl_add_u64 v[24:25], v[24:25], 0, v[2:3]
	global_load_dwordx4 v[54:57], v[24:25], off
	v_add_u32_e32 v24, 0xc00, v1
	v_ashrrev_i32_e32 v24, 10, v24
	v_ashrrev_i32_e32 v25, 31, v24
	v_lshl_add_u64 v[26:27], s[0:1], 0, v[24:25]
	v_lshlrev_b64 v[26:27], 13, v[26:27]
	v_lshl_add_u64 v[26:27], v[6:7], 0, v[26:27]
	v_lshl_add_u64 v[26:27], v[26:27], 0, v[2:3]
	global_load_dwordx4 v[58:61], v[26:27], off
	v_add_u32_e32 v27, 0xe00, v1
	v_ashrrev_i32_e32 v26, 10, v27
	v_and_b32_e32 v27, 0x200, v27
	v_cmp_eq_u32_e64 s[8:9], 0, v27
	v_ashrrev_i32_e32 v27, 31, v26
	v_lshl_add_u64 v[30:31], s[0:1], 0, v[26:27]
	v_cndmask_b32_e64 v29, v94, v95, s[8:9]
	v_cndmask_b32_e64 v28, v96, v97, s[8:9]
	v_lshlrev_b64 v[30:31], 13, v[30:31]
	v_lshl_add_u64 v[30:31], v[28:29], 0, v[30:31]
	v_lshl_add_u64 v[30:31], v[30:31], 0, v[2:3]
	global_load_dwordx4 v[62:65], v[30:31], off
	v_add_u32_e32 v30, 0x1000, v1
	v_ashrrev_i32_e32 v30, 10, v30
	v_ashrrev_i32_e32 v31, 31, v30
	v_lshl_add_u64 v[32:33], s[0:1], 0, v[30:31]
	v_lshlrev_b64 v[32:33], 13, v[32:33]
	v_lshl_add_u64 v[32:33], v[6:7], 0, v[32:33]
	v_lshl_add_u64 v[32:33], v[32:33], 0, v[2:3]
	global_load_dwordx4 v[66:69], v[32:33], off
	v_add_u32_e32 v33, 0x1200, v1
	v_add_u32_e32 v82, 0x1800, v1
	v_add_u32_e32 v86, 0x1a00, v1
	v_add_u32_e32 v90, 0x1c00, v1
	v_add_u32_e32 v115, 0x1e00, v1
	v_ashrrev_i32_e32 v32, 10, v33
	v_and_b32_e32 v33, 0x200, v33
	v_ashrrev_i32_e32 v102, 10, v78
	v_and_b32_e32 v78, 0x200, v78
	v_ashrrev_i32_e32 v106, 10, v82
	v_ashrrev_i32_e32 v108, 10, v86
	v_and_b32_e32 v86, 0x200, v86
	v_ashrrev_i32_e32 v112, 10, v90
	v_ashrrev_i32_e32 v114, 10, v115
	v_and_b32_e32 v115, 0x200, v115
	v_cmp_eq_u32_e64 s[10:11], 0, v33
	v_ashrrev_i32_e32 v33, 31, v32
	v_cmp_eq_u32_e64 s[12:13], 0, v78
	v_ashrrev_i32_e32 v103, 31, v102
	v_ashrrev_i32_e32 v107, 31, v106
	v_cmp_eq_u32_e64 s[14:15], 0, v86
	v_ashrrev_i32_e32 v109, 31, v108
	v_ashrrev_i32_e32 v113, 31, v112
	v_cmp_eq_u32_e64 s[16:17], 0, v115
	v_ashrrev_i32_e32 v115, 31, v114
	v_cndmask_b32_e64 v99, v94, v95, s[10:11]
	v_lshl_add_u64 v[70:71], s[0:1], 0, v[32:33]
	v_cndmask_b32_e64 v105, v94, v95, s[12:13]
	v_lshl_add_u64 v[78:79], s[0:1], 0, v[102:103]
	v_lshl_add_u64 v[82:83], s[0:1], 0, v[106:107]
	v_cndmask_b32_e64 v111, v94, v95, s[14:15]
	v_lshl_add_u64 v[86:87], s[0:1], 0, v[108:109]
	v_lshl_add_u64 v[90:91], s[0:1], 0, v[112:113]
	v_cndmask_b32_e64 v117, v94, v95, s[16:17]
	v_lshl_add_u64 v[94:95], s[0:1], 0, v[114:115]
	v_cndmask_b32_e64 v98, v96, v97, s[10:11]
	v_lshlrev_b64 v[70:71], 13, v[70:71]
	v_cndmask_b32_e64 v104, v96, v97, s[12:13]
	v_lshlrev_b64 v[78:79], 13, v[78:79]
	v_lshlrev_b64 v[82:83], 13, v[82:83]
	v_cndmask_b32_e64 v110, v96, v97, s[14:15]
	v_lshlrev_b64 v[86:87], 13, v[86:87]
	v_lshlrev_b64 v[90:91], 13, v[90:91]
	v_cndmask_b32_e64 v116, v96, v97, s[16:17]
	v_lshlrev_b64 v[94:95], 13, v[94:95]
	v_lshl_add_u64 v[70:71], v[98:99], 0, v[70:71]
	v_lshl_add_u64 v[78:79], v[104:105], 0, v[78:79]
	v_lshl_add_u64 v[82:83], v[6:7], 0, v[82:83]
	v_lshl_add_u64 v[86:87], v[110:111], 0, v[86:87]
	v_lshl_add_u64 v[90:91], v[6:7], 0, v[90:91]
	v_lshl_add_u64 v[94:95], v[116:117], 0, v[94:95]
	v_lshl_add_u64 v[70:71], v[70:71], 0, v[2:3]
	v_lshl_add_u64 v[78:79], v[78:79], 0, v[2:3]
	v_lshl_add_u64 v[82:83], v[82:83], 0, v[2:3]
	v_lshl_add_u64 v[86:87], v[86:87], 0, v[2:3]
	v_lshl_add_u64 v[90:91], v[90:91], 0, v[2:3]
	v_lshl_add_u64 v[94:95], v[94:95], 0, v[2:3]
	global_load_dwordx4 v[70:73], v[70:71], off
	v_and_b32_e32 v121, 0x1ff, v1
	global_load_dwordx4 v[78:81], v[78:79], off
	v_ashrrev_i32_e32 v118, 6, v1
	global_load_dwordx4 v[82:85], v[82:83], off
	v_and_b32_e32 v119, 31, v1
	global_load_dwordx4 v[86:89], v[86:87], off
	v_bfe_u32 v2, v1, 5, 1
	global_load_dwordx4 v[90:93], v[90:91], off
	v_lshlrev_b32_e32 v144, 4, v121
	global_load_dwordx4 v[94:97], v[94:95], off
	v_bfe_u32 v1, v1, 3, 6
	v_and_b32_e32 v120, 0x70, v120
	s_movk_i32 s20, 0x90
	v_add_u32_e32 v121, 0x2400, v144
	v_mad_u32_u24 v1, v1, s20, v120
	v_cmp_gt_i32_e64 s[0:1], 2, v118
	v_lshl_or_b32 v146, v118, 5, v119
	v_lshlrev_b32_e32 v118, 9, v2
	v_cndmask_b32_e64 v157, v121, v1, s[4:5]
	s_add_i32 s4, 0, 0x13400
	v_lshlrev_b32_e32 v149, 3, v2
	v_add_u32_e32 v179, s4, v118
	s_add_i32 s4, 0, 0x11000
	v_add_u32_e32 v180, s4, v149
	s_add_i32 s4, 0, 0x17800
	v_add_u32_e32 v181, s4, v118
	s_add_i32 s4, 0, 0x15400
	v_add_u32_e32 v182, s4, v149
	s_add_i32 s4, 0, 0x1bc00
	v_add_u32_e32 v183, s4, v118
	s_add_i32 s4, 0, 0x19800
	v_add_u32_e32 v184, s4, v149
	s_add_i32 s4, 0, 0x20000
	v_add_u32_e32 v185, s4, v118
	s_add_i32 s4, 0, 0x1dc00
	v_add_u32_e32 v186, s4, v149
	s_mov_b32 s4, s22
	s_movk_i32 s21, 0x4400
	v_writelane_b32 v253, s4, 0
	v_mad_i32_i24 v152, v4, s21, 0
	v_lshlrev_b64 v[4:5], 13, v[4:5]
	v_writelane_b32 v253, s5, 1
	s_lshl_b64 s[4:5], s[22:23], 20
	v_lshl_add_u64 v[4:5], s[4:5], 0, v[4:5]
	v_mad_i32_i24 v153, v10, s21, 0
	v_mad_i32_i24 v155, v12, s21, 0
	v_mad_i32_i24 v156, v16, s21, 0
	v_mad_i32_i24 v158, v18, s21, 0
	v_mad_i32_i24 v159, v22, s21, 0
	v_mad_i32_i24 v161, v24, s21, 0
	v_mad_i32_i24 v162, v26, s21, 0
	v_mad_i32_i24 v164, v30, s21, 0
	v_mad_i32_i24 v165, v32, s21, 0
	v_mad_i32_i24 v168, v100, s21, 0
	v_mad_i32_i24 v169, v102, s21, 0
	v_mad_i32_i24 v171, v106, s21, 0
	v_mad_i32_i24 v172, v108, s21, 0
	v_mad_i32_i24 v174, v112, s21, 0
	v_mad_i32_i24 v175, v114, s21, 0
	v_lshlrev_b64 v[114:115], 13, v[114:115]
	v_lshlrev_b64 v[112:113], 13, v[112:113]
	v_lshlrev_b64 v[108:109], 13, v[108:109]
	v_lshlrev_b64 v[106:107], 13, v[106:107]
	v_lshlrev_b64 v[102:103], 13, v[102:103]
	v_lshlrev_b64 v[100:101], 13, v[100:101]
	v_lshlrev_b64 v[32:33], 13, v[32:33]
	v_lshlrev_b64 v[30:31], 13, v[30:31]
	v_lshlrev_b64 v[26:27], 13, v[26:27]
	v_lshlrev_b64 v[24:25], 13, v[24:25]
	v_lshlrev_b64 v[22:23], 13, v[22:23]
	v_lshlrev_b64 v[18:19], 13, v[18:19]
	v_lshlrev_b64 v[16:17], 13, v[16:17]
	v_lshlrev_b64 v[12:13], 13, v[12:13]
	v_lshlrev_b64 v[10:11], 13, v[10:11]
	v_or_b32_e32 v4, v4, v144
	v_cndmask_b32_e64 v160, v121, v1, s[6:7]
	v_lshl_add_u64 v[114:115], s[4:5], 0, v[114:115]
	s_mov_b64 s[6:7], 0x10000
	v_lshl_add_u64 v[112:113], s[4:5], 0, v[112:113]
	v_lshl_add_u64 v[108:109], s[4:5], 0, v[108:109]
	v_lshl_add_u64 v[106:107], s[4:5], 0, v[106:107]
	v_lshl_add_u64 v[102:103], s[4:5], 0, v[102:103]
	v_lshl_add_u64 v[100:101], s[4:5], 0, v[100:101]
	v_lshl_add_u64 v[32:33], s[4:5], 0, v[32:33]
	v_lshl_add_u64 v[30:31], s[4:5], 0, v[30:31]
	v_lshl_add_u64 v[26:27], s[4:5], 0, v[26:27]
	v_lshl_add_u64 v[24:25], s[4:5], 0, v[24:25]
	v_lshl_add_u64 v[22:23], s[4:5], 0, v[22:23]
	v_lshl_add_u64 v[18:19], s[4:5], 0, v[18:19]
	v_lshl_add_u64 v[16:17], s[4:5], 0, v[16:17]
	v_lshl_add_u64 v[12:13], s[4:5], 0, v[12:13]
	v_lshl_add_u64 v[10:11], s[4:5], 0, v[10:11]
	v_lshl_add_u64 v[4:5], v[6:7], 0, v[4:5]
	v_ashrrev_i32_e32 v147, 31, v146
	v_or_b32_e32 v114, v114, v144
	v_or_b32_e32 v112, v112, v144
	v_or_b32_e32 v108, v108, v144
	v_or_b32_e32 v106, v106, v144
	v_or_b32_e32 v102, v102, v144
	v_or_b32_e32 v100, v100, v144
	v_or_b32_e32 v32, v32, v144
	v_or_b32_e32 v30, v30, v144
	v_or_b32_e32 v26, v26, v144
	v_or_b32_e32 v24, v24, v144
	v_or_b32_e32 v22, v22, v144
	v_or_b32_e32 v18, v18, v144
	v_or_b32_e32 v16, v16, v144
	v_or_b32_e32 v12, v12, v144
	v_or_b32_e32 v10, v10, v144
	v_lshl_add_u64 v[144:145], v[4:5], 0, s[6:7]
	v_lshlrev_b64 v[4:5], 7, v[146:147]
	v_lshl_add_u64 v[4:5], s[4:5], 0, v[4:5]
	v_lshlrev_b32_e32 v148, 1, v146
	v_add_u32_e32 v120, 0, v149
	v_mul_u32_u24_e32 v2, 0x1f8, v2
	v_lshl_add_u64 v[32:33], v[98:99], 0, v[32:33]
	v_lshl_add_u64 v[30:31], v[6:7], 0, v[30:31]
	v_lshl_add_u64 v[26:27], v[28:29], 0, v[26:27]
	v_lshl_add_u64 v[24:25], v[6:7], 0, v[24:25]
	v_lshl_add_u64 v[20:21], v[20:21], 0, v[22:23]
	v_lshl_add_u64 v[18:19], v[6:7], 0, v[18:19]
	v_lshl_add_u64 v[14:15], v[14:15], 0, v[16:17]
	v_lshl_add_u64 v[12:13], v[6:7], 0, v[12:13]
	v_lshl_add_u64 v[8:9], v[8:9], 0, v[10:11]
	v_or_b32_e32 v4, v4, v149
	v_mov_b32_e32 v16, v3
	v_mov_b32_e32 v17, v3
	v_cndmask_b32_e32 v166, v121, v1, vcc
	v_cndmask_b32_e32 v154, v1, v121, vcc
	v_cndmask_b32_e64 v163, v121, v1, s[8:9]
	v_cndmask_b32_e64 v167, v121, v1, s[10:11]
	v_cndmask_b32_e64 v170, v121, v1, s[12:13]
	v_cndmask_b32_e64 v173, v121, v1, s[14:15]
	v_cndmask_b32_e64 v176, v121, v1, s[16:17]
	v_add_u32_e32 v177, 0, v118
	v_mul_u32_u24_e32 v178, 0x90, v119
	v_add3_u32 v150, v120, v2, v148
	v_lshl_add_u64 v[114:115], v[116:117], 0, v[114:115]
	v_lshl_add_u64 v[112:113], v[6:7], 0, v[112:113]
	v_lshl_add_u64 v[108:109], v[110:111], 0, v[108:109]
	v_lshl_add_u64 v[106:107], v[6:7], 0, v[106:107]
	v_lshl_add_u64 v[102:103], v[104:105], 0, v[102:103]
	v_lshl_add_u64 v[100:101], v[6:7], 0, v[100:101]
	v_lshl_add_u64 v[126:127], v[32:33], 0, s[6:7]
	v_lshl_add_u64 v[128:129], v[30:31], 0, s[6:7]
	v_lshl_add_u64 v[130:131], v[26:27], 0, s[6:7]
	v_lshl_add_u64 v[132:133], v[24:25], 0, s[6:7]
	v_lshl_add_u64 v[134:135], v[20:21], 0, s[6:7]
	v_lshl_add_u64 v[136:137], v[18:19], 0, s[6:7]
	v_lshl_add_u64 v[138:139], v[14:15], 0, s[6:7]
	v_lshl_add_u64 v[140:141], v[12:13], 0, s[6:7]
	v_lshl_add_u64 v[142:143], v[8:9], 0, s[6:7]
	v_lshl_add_u64 v[146:147], s[48:49], 0, v[4:5]
	v_mov_b32_e32 v2, v3
	v_mov_b32_e32 v4, v3
	v_mov_b32_e32 v5, v3
	v_mov_b32_e32 v6, v3
	v_mov_b32_e32 v7, v3
	v_mov_b32_e32 v8, v3
	v_mov_b32_e32 v9, v3
	v_mov_b32_e32 v10, v3
	v_mov_b32_e32 v11, v3
	v_mov_b32_e32 v12, v3
	v_mov_b32_e32 v13, v3
	v_mov_b32_e32 v14, v3
	v_mov_b32_e32 v15, v3
	v_mov_b64_e32 v[32:33], v[16:17]
	v_mad_u32_u24 v1, v119, s20, v120
	v_add_u32_e32 v151, 0xf000, v150
	v_lshl_add_u64 v[114:115], v[114:115], 0, s[6:7]
	v_lshl_add_u64 v[116:117], v[112:113], 0, s[6:7]
	v_lshl_add_u64 v[118:119], v[108:109], 0, s[6:7]
	v_lshl_add_u64 v[120:121], v[106:107], 0, s[6:7]
	v_lshl_add_u64 v[122:123], v[102:103], 0, s[6:7]
	v_lshl_add_u64 v[124:125], v[100:101], 0, s[6:7]
	s_mov_b64 s[4:5], 0
	v_add_u32_e32 v152, v152, v166
	v_add_u32_e32 v153, v153, v154
	v_add_u32_e32 v154, v155, v166
	v_add_u32_e32 v155, v156, v157
	v_add_u32_e32 v156, v158, v166
	v_add_u32_e32 v157, v159, v160
	v_add_u32_e32 v158, v161, v166
	v_add_u32_e32 v159, v162, v163
	v_add_u32_e32 v160, v164, v166
	v_add_u32_e32 v161, v165, v167
	v_add_u32_e32 v162, v168, v166
	v_add_u32_e32 v163, v169, v170
	v_add_u32_e32 v164, v171, v166
	v_add_u32_e32 v165, v172, v173
	v_add_u32_e32 v166, v174, v166
	v_add_u32_e32 v167, v175, v176
	v_add_u32_e32 v168, v177, v148
	s_mov_b32 s8, 0x14802000
	s_mov_b32 s9, 0x14804000
	s_mov_b32 s10, 0x14806000
	s_mov_b32 s11, 0x14808000
	v_add_u32_e32 v169, v179, v148
	v_add_u32_e32 v170, v180, v178
	s_mov_b32 s12, 0x1480a000
	v_add_u32_e32 v171, v181, v148
	v_add_u32_e32 v172, v182, v178
	s_mov_b32 s13, 0x1480c000
	v_add_u32_e32 v173, v183, v148
	v_add_u32_e32 v174, v184, v178
	s_mov_b32 s14, 0x1480e000
	v_add_u32_e32 v175, v185, v148
	v_add_u32_e32 v176, v186, v178
	v_mov_b64_e32 v[30:31], v[14:15]
	v_mov_b64_e32 v[28:29], v[12:13]
	v_mov_b64_e32 v[26:27], v[10:11]
	v_mov_b64_e32 v[24:25], v[8:9]
	v_mov_b64_e32 v[22:23], v[6:7]
	v_mov_b64_e32 v[20:21], v[4:5]
	v_mov_b64_e32 v[18:19], v[2:3]
	v_mov_b32_e32 v212, 0
	v_mov_b32_e32 v213, 0
	v_mov_b32_e32 v214, 0
	v_mov_b32_e32 v215, 0
	v_mov_b32_e32 v216, 0
	v_mov_b32_e32 v217, 0
	v_mov_b32_e32 v218, 0
	v_mov_b32_e32 v219, 0
	v_mov_b32_e32 v220, 0
	v_mov_b32_e32 v221, 0
	v_mov_b32_e32 v222, 0
	v_mov_b32_e32 v223, 0
	v_mov_b32_e32 v224, 0
	v_mov_b32_e32 v225, 0
	v_mov_b32_e32 v226, 0
	v_mov_b32_e32 v227, 0
	v_mov_b32_e32 v228, 0
	v_mov_b32_e32 v229, 0
	v_mov_b32_e32 v230, 0
	v_mov_b32_e32 v231, 0
	v_mov_b32_e32 v232, 0
	v_mov_b32_e32 v233, 0
	v_mov_b32_e32 v234, 0
	v_mov_b32_e32 v235, 0
	v_mov_b32_e32 v236, 0
	v_mov_b32_e32 v237, 0
	v_mov_b32_e32 v238, 0
	v_mov_b32_e32 v239, 0
	v_mov_b32_e32 v240, 0
	v_mov_b32_e32 v241, 0
	v_mov_b32_e32 v242, 0
	v_mov_b32_e32 v243, 0
	v_and_b32_e32 v187, 31, v0
	v_bfe_u32 v247, v0, 5, 1
	v_mul_u32_u24_e32 v250, 0x70, v187
	v_mul_u32_u24_e32 v251, 0x1f8, v247
	v_sub_u32_e32 v250, v251, v250
	v_ashrrev_i32_e32 v251, 31, v250
	v_lshl_add_u64 v[250:251], v[146:147], 0, v[250:251]
	v_mul_u32_u24_e32 v187, 0x90, v187
	v_lshl_add_u32 v187, v247, 3, v187
	v_lshrrev_b32_e32 v247, 6, v0
	v_mul_u32_u24_e32 v247, 0x1200, v247
	v_add_u32_e32 v247, 0x24000, v247
	v_add_u32_e32 v187, v187, v247
	v_bfe_u32 v244, v0, 3, 3
	v_mul_u32_u24_e32 v244, 0x90, v244
	v_add_u32_e32 v247, v247, v244
	v_and_b32_e32 v244, 7, v0
	v_lshl_add_u32 v247, v244, 4, v247
	v_add_u32_e32 v244, 52224, v168
	v_add_u32_e32 v245, 104448, v168
	v_add_u32_e32 v246, 69632, v1
	s_branch .LBB0_1923

.LBB0_1925:
	s_and_saveexec_b64 s[6:7], s[0:1]
	s_cbranch_execz .LBB0_1922
	v_lshl_add_u64 v[148:149], v[250:251], 0, s[4:5]
	ds_read_b64 v[178:179], v1 offset:0
	ds_read_b64 v[180:181], v1 offset:16
	ds_read_b64 v[182:183], v1 offset:32
	ds_read_b64 v[184:185], v1 offset:48
	ds_read_b64 v[188:189], v1 offset:64
	ds_read_b64 v[190:191], v1 offset:80
	ds_read_b64 v[192:193], v1 offset:96
	ds_read_b64 v[194:195], v1 offset:112
	ds_read_b64 v[196:197], v1 offset:4608
	ds_read_b64 v[198:199], v1 offset:4624
	ds_read_b64 v[200:201], v1 offset:4640
	ds_read_b64 v[202:203], v1 offset:4656
	ds_read_b64 v[204:205], v1 offset:4672
	ds_read_b64 v[206:207], v1 offset:4688
	ds_read_b64 v[208:209], v1 offset:4704
	ds_read_b64 v[210:211], v1 offset:4720
	ds_read_u16_d16_hi v212, v168 offset:9216
	ds_read_u16_d16_hi v213, v168 offset:9344
	ds_read_u16_d16_hi v214, v168 offset:9472
	ds_read_u16_d16_hi v215, v168 offset:9600
	ds_read_u16_d16_hi v216, v168 offset:10240
	ds_read_u16_d16_hi v217, v168 offset:10368
	ds_read_u16_d16_hi v218, v168 offset:10496
	ds_read_u16_d16_hi v219, v168 offset:10624
	ds_read_u16_d16_hi v220, v168 offset:11264
	ds_read_u16_d16_hi v221, v168 offset:11392
	ds_read_u16_d16_hi v222, v168 offset:11520
	ds_read_u16_d16_hi v223, v168 offset:11648
	ds_read_u16_d16_hi v224, v168 offset:12288
	ds_read_u16_d16_hi v225, v168 offset:12416
	ds_read_u16_d16_hi v226, v168 offset:12544
	ds_read_u16_d16_hi v227, v168 offset:12672
	ds_read_u16_d16_hi v228, v168 offset:13312
	ds_read_u16_d16_hi v229, v168 offset:13440
	ds_read_u16_d16_hi v230, v168 offset:13568
	ds_read_u16_d16_hi v231, v168 offset:13696
	ds_read_u16_d16_hi v232, v168 offset:14336
	ds_read_u16_d16_hi v233, v168 offset:14464
	ds_read_u16_d16_hi v234, v168 offset:14592
	ds_read_u16_d16_hi v235, v168 offset:14720
	ds_read_u16_d16_hi v236, v168 offset:15360
	ds_read_u16_d16_hi v237, v168 offset:15488
	ds_read_u16_d16_hi v238, v168 offset:15616
	ds_read_u16_d16_hi v239, v168 offset:15744
	ds_read_u16_d16_hi v240, v168 offset:16384
	ds_read_u16_d16_hi v241, v168 offset:16512
	ds_read_u16_d16_hi v242, v168 offset:16640
	ds_read_u16_d16_hi v243, v168 offset:16768
	v_cvt_pk_bf16_f32 v110, v18, v19
	v_cvt_pk_bf16_f32 v111, v20, v21
	v_cvt_pk_bf16_f32 v112, v22, v23
	v_cvt_pk_bf16_f32 v113, v24, v25
	v_cvt_pk_bf16_f32 v106, v26, v27
	v_cvt_pk_bf16_f32 v107, v28, v29
	v_cvt_pk_bf16_f32 v108, v30, v31
	v_cvt_pk_bf16_f32 v109, v32, v33
	v_cvt_pk_bf16_f32 v102, v2, v3
	v_cvt_pk_bf16_f32 v103, v4, v5
	v_cvt_pk_bf16_f32 v104, v6, v7
	v_cvt_pk_bf16_f32 v105, v8, v9
	v_cvt_pk_bf16_f32 v98, v10, v11
	v_cvt_pk_bf16_f32 v99, v12, v13
	v_cvt_pk_bf16_f32 v100, v14, v15
	v_cvt_pk_bf16_f32 v101, v16, v17
	v_add_co_u32_e32 v248, vcc, 0x14800000, v148
	s_nop 1
	v_addc_co_u32_e32 v249, vcc, 0, v149, vcc
	s_waitcnt lgkmcnt(0)
	v_mfma_f32_32x32x16_bf16 v[18:33], v[178:181], v[110:113], v[212:227]
	ds_read_b64 v[178:179], v1 offset:17408
	ds_read_b64 v[180:181], v1 offset:17424
	v_mfma_f32_32x32x16_bf16 v[2:17], v[196:199], v[110:113], v[228:243]
	ds_read_b64 v[196:197], v1 offset:22016
	ds_read_b64 v[198:199], v1 offset:22032
	v_mfma_f32_32x32x16_bf16 v[18:33], v[182:185], v[106:109], v[18:33]
	ds_read_b64 v[182:183], v1 offset:17440
	ds_read_b64 v[184:185], v1 offset:17456
	v_mfma_f32_32x32x16_bf16 v[2:17], v[200:203], v[106:109], v[2:17]
	ds_read_b64 v[200:201], v1 offset:22048
	ds_read_b64 v[202:203], v1 offset:22064
	ds_read_u16_d16_hi v212, v168 offset:26624
	ds_read_u16_d16_hi v213, v168 offset:26752
	ds_read_u16_d16_hi v214, v168 offset:26880
	ds_read_u16_d16_hi v215, v168 offset:27008
	ds_read_u16_d16_hi v216, v168 offset:27648
	ds_read_u16_d16_hi v217, v168 offset:27776
	ds_read_u16_d16_hi v218, v168 offset:27904
	ds_read_u16_d16_hi v219, v168 offset:28032
	v_mfma_f32_32x32x16_bf16 v[18:33], v[188:191], v[102:105], v[18:33]
	ds_read_b64 v[188:189], v1 offset:17472
	ds_read_b64 v[190:191], v1 offset:17488
	ds_read_u16_d16_hi v220, v168 offset:28672
	ds_read_u16_d16_hi v221, v168 offset:28800
	ds_read_u16_d16_hi v222, v168 offset:28928
	ds_read_u16_d16_hi v223, v168 offset:29056
	ds_read_u16_d16_hi v224, v168 offset:29696
	ds_read_u16_d16_hi v225, v168 offset:29824
	ds_read_u16_d16_hi v226, v168 offset:29952
	ds_read_u16_d16_hi v227, v168 offset:30080
	v_mfma_f32_32x32x16_bf16 v[2:17], v[204:207], v[102:105], v[2:17]
	ds_read_b64 v[204:205], v1 offset:22080
	ds_read_b64 v[206:207], v1 offset:22096
	ds_read_u16_d16_hi v228, v168 offset:30720
	ds_read_u16_d16_hi v229, v168 offset:30848
	ds_read_u16_d16_hi v230, v168 offset:30976
	ds_read_u16_d16_hi v231, v168 offset:31104
	ds_read_u16_d16_hi v232, v168 offset:31744
	ds_read_u16_d16_hi v233, v168 offset:31872
	ds_read_u16_d16_hi v234, v168 offset:32000
	ds_read_u16_d16_hi v235, v168 offset:32128
	v_mfma_f32_32x32x16_bf16 v[18:33], v[192:195], v[98:101], v[18:33]
	ds_read_b64 v[192:193], v1 offset:17504
	ds_read_b64 v[194:195], v1 offset:17520
	ds_read_u16_d16_hi v236, v168 offset:32768
	ds_read_u16_d16_hi v237, v168 offset:32896
	ds_read_u16_d16_hi v238, v168 offset:33024
	ds_read_u16_d16_hi v239, v168 offset:33152
	ds_read_u16_d16_hi v240, v168 offset:33792
	ds_read_u16_d16_hi v241, v168 offset:33920
	ds_read_u16_d16_hi v242, v168 offset:34048
	ds_read_u16_d16_hi v243, v168 offset:34176
	v_mfma_f32_32x32x16_bf16 v[2:17], v[208:211], v[98:101], v[2:17]
	ds_read_b64 v[208:209], v1 offset:22112
	ds_read_b64 v[210:211], v1 offset:22128
	ds_write_b64 v187, v[110:111]
	ds_write_b64 v187, v[112:113] offset:16
	ds_write_b64 v187, v[106:107] offset:32
	ds_write_b64 v187, v[108:109] offset:48
	ds_write_b64 v187, v[102:103] offset:64
	ds_write_b64 v187, v[104:105] offset:80
	ds_write_b64 v187, v[98:99] offset:96
	ds_write_b64 v187, v[100:101] offset:112
	ds_read_b128 v[110:113], v247
	ds_read_b128 v[106:109], v247 offset:1152
	ds_read_b128 v[102:105], v247 offset:2304
	ds_read_b128 v[98:101], v247 offset:3456
	s_waitcnt lgkmcnt(0)
	global_store_dwordx4 v[248:249], v[110:113], off
	global_store_dwordx4 v[248:249], v[106:109], off offset:1024
	global_store_dwordx4 v[248:249], v[102:105], off offset:2048
	global_store_dwordx4 v[248:249], v[98:101], off offset:3072
	s_nop 1
	v_cvt_pk_bf16_f32 v110, v18, v19
	v_cvt_pk_bf16_f32 v111, v20, v21
	v_cvt_pk_bf16_f32 v112, v22, v23
	v_cvt_pk_bf16_f32 v113, v24, v25
	v_cvt_pk_bf16_f32 v106, v26, v27
	v_cvt_pk_bf16_f32 v107, v28, v29
	v_cvt_pk_bf16_f32 v108, v30, v31
	v_cvt_pk_bf16_f32 v109, v32, v33
	v_cvt_pk_bf16_f32 v102, v2, v3
	v_cvt_pk_bf16_f32 v103, v4, v5
	v_cvt_pk_bf16_f32 v104, v6, v7
	v_cvt_pk_bf16_f32 v105, v8, v9
	v_cvt_pk_bf16_f32 v98, v10, v11
	v_cvt_pk_bf16_f32 v99, v12, v13
	v_cvt_pk_bf16_f32 v100, v14, v15
	v_cvt_pk_bf16_f32 v101, v16, v17
	v_add_co_u32_e32 v248, vcc, s8, v148
	s_nop 1
	v_addc_co_u32_e32 v249, vcc, 0, v149, vcc
	s_waitcnt lgkmcnt(0)
	v_mfma_f32_32x32x16_bf16 v[18:33], v[178:181], v[110:113], v[212:227]
	ds_read_b64 v[178:179], v1 offset:34816
	ds_read_b64 v[180:181], v1 offset:34832
	v_mfma_f32_32x32x16_bf16 v[2:17], v[196:199], v[110:113], v[228:243]
	ds_read_b64 v[196:197], v1 offset:39424
	ds_read_b64 v[198:199], v1 offset:39440
	v_mfma_f32_32x32x16_bf16 v[18:33], v[182:185], v[106:109], v[18:33]
	ds_read_b64 v[182:183], v1 offset:34848
	ds_read_b64 v[184:185], v1 offset:34864
	v_mfma_f32_32x32x16_bf16 v[2:17], v[200:203], v[106:109], v[2:17]
	ds_read_b64 v[200:201], v1 offset:39456
	ds_read_b64 v[202:203], v1 offset:39472
	ds_read_u16_d16_hi v212, v168 offset:44032
	ds_read_u16_d16_hi v213, v168 offset:44160
	ds_read_u16_d16_hi v214, v168 offset:44288
	ds_read_u16_d16_hi v215, v168 offset:44416
	ds_read_u16_d16_hi v216, v168 offset:45056
	ds_read_u16_d16_hi v217, v168 offset:45184
	ds_read_u16_d16_hi v218, v168 offset:45312
	ds_read_u16_d16_hi v219, v168 offset:45440
	v_mfma_f32_32x32x16_bf16 v[18:33], v[188:191], v[102:105], v[18:33]
	ds_read_b64 v[188:189], v1 offset:34880
	ds_read_b64 v[190:191], v1 offset:34896
	ds_read_u16_d16_hi v220, v168 offset:46080
	ds_read_u16_d16_hi v221, v168 offset:46208
	ds_read_u16_d16_hi v222, v168 offset:46336
	ds_read_u16_d16_hi v223, v168 offset:46464
	ds_read_u16_d16_hi v224, v168 offset:47104
	ds_read_u16_d16_hi v225, v168 offset:47232
	ds_read_u16_d16_hi v226, v168 offset:47360
	ds_read_u16_d16_hi v227, v168 offset:47488
	v_mfma_f32_32x32x16_bf16 v[2:17], v[204:207], v[102:105], v[2:17]
	ds_read_b64 v[204:205], v1 offset:39488
	ds_read_b64 v[206:207], v1 offset:39504
	ds_read_u16_d16_hi v228, v168 offset:48128
	ds_read_u16_d16_hi v229, v168 offset:48256
	ds_read_u16_d16_hi v230, v168 offset:48384
	ds_read_u16_d16_hi v231, v168 offset:48512
	ds_read_u16_d16_hi v232, v168 offset:49152
	ds_read_u16_d16_hi v233, v168 offset:49280
	ds_read_u16_d16_hi v234, v168 offset:49408
	ds_read_u16_d16_hi v235, v168 offset:49536
	v_mfma_f32_32x32x16_bf16 v[18:33], v[192:195], v[98:101], v[18:33]
	ds_read_b64 v[192:193], v1 offset:34912
	ds_read_b64 v[194:195], v1 offset:34928
	ds_read_u16_d16_hi v236, v168 offset:50176
	ds_read_u16_d16_hi v237, v168 offset:50304
	ds_read_u16_d16_hi v238, v168 offset:50432
	ds_read_u16_d16_hi v239, v168 offset:50560
	ds_read_u16_d16_hi v240, v168 offset:51200
	ds_read_u16_d16_hi v241, v168 offset:51328
	ds_read_u16_d16_hi v242, v168 offset:51456
	ds_read_u16_d16_hi v243, v168 offset:51584
	v_mfma_f32_32x32x16_bf16 v[2:17], v[208:211], v[98:101], v[2:17]
	ds_read_b64 v[208:209], v1 offset:39520
	ds_read_b64 v[210:211], v1 offset:39536
	ds_write_b64 v187, v[110:111]
	ds_write_b64 v187, v[112:113] offset:16
	ds_write_b64 v187, v[106:107] offset:32
	ds_write_b64 v187, v[108:109] offset:48
	ds_write_b64 v187, v[102:103] offset:64
	ds_write_b64 v187, v[104:105] offset:80
	ds_write_b64 v187, v[98:99] offset:96
	ds_write_b64 v187, v[100:101] offset:112
	ds_read_b128 v[110:113], v247
	ds_read_b128 v[106:109], v247 offset:1152
	ds_read_b128 v[102:105], v247 offset:2304
	ds_read_b128 v[98:101], v247 offset:3456
	s_waitcnt lgkmcnt(0)
	global_store_dwordx4 v[248:249], v[110:113], off
	global_store_dwordx4 v[248:249], v[106:109], off offset:1024
	global_store_dwordx4 v[248:249], v[102:105], off offset:2048
	global_store_dwordx4 v[248:249], v[98:101], off offset:3072
	s_nop 1
	v_cvt_pk_bf16_f32 v110, v18, v19
	v_cvt_pk_bf16_f32 v111, v20, v21
	v_cvt_pk_bf16_f32 v112, v22, v23
	v_cvt_pk_bf16_f32 v113, v24, v25
	v_cvt_pk_bf16_f32 v106, v26, v27
	v_cvt_pk_bf16_f32 v107, v28, v29
	v_cvt_pk_bf16_f32 v108, v30, v31
	v_cvt_pk_bf16_f32 v109, v32, v33
	v_cvt_pk_bf16_f32 v102, v2, v3
	v_cvt_pk_bf16_f32 v103, v4, v5
	v_cvt_pk_bf16_f32 v104, v6, v7
	v_cvt_pk_bf16_f32 v105, v8, v9
	v_cvt_pk_bf16_f32 v98, v10, v11
	v_cvt_pk_bf16_f32 v99, v12, v13
	v_cvt_pk_bf16_f32 v100, v14, v15
	v_cvt_pk_bf16_f32 v101, v16, v17
	v_add_co_u32_e32 v248, vcc, s9, v148
	s_nop 1
	v_addc_co_u32_e32 v249, vcc, 0, v149, vcc
	s_waitcnt lgkmcnt(0)
	v_mfma_f32_32x32x16_bf16 v[18:33], v[178:181], v[110:113], v[212:227]
	ds_read_b64 v[178:179], v1 offset:52224
	ds_read_b64 v[180:181], v1 offset:52240
	v_mfma_f32_32x32x16_bf16 v[2:17], v[196:199], v[110:113], v[228:243]
	ds_read_b64 v[196:197], v1 offset:56832
	ds_read_b64 v[198:199], v1 offset:56848
	v_mfma_f32_32x32x16_bf16 v[18:33], v[182:185], v[106:109], v[18:33]
	ds_read_b64 v[182:183], v1 offset:52256
	ds_read_b64 v[184:185], v1 offset:52272
	v_mfma_f32_32x32x16_bf16 v[2:17], v[200:203], v[106:109], v[2:17]
	ds_read_b64 v[200:201], v1 offset:56864
	ds_read_b64 v[202:203], v1 offset:56880
	ds_read_u16_d16_hi v212, v244 offset:9216
	ds_read_u16_d16_hi v213, v244 offset:9344
	ds_read_u16_d16_hi v214, v244 offset:9472
	ds_read_u16_d16_hi v215, v244 offset:9600
	ds_read_u16_d16_hi v216, v244 offset:10240
	ds_read_u16_d16_hi v217, v244 offset:10368
	ds_read_u16_d16_hi v218, v244 offset:10496
	ds_read_u16_d16_hi v219, v244 offset:10624
	v_mfma_f32_32x32x16_bf16 v[18:33], v[188:191], v[102:105], v[18:33]
	ds_read_b64 v[188:189], v1 offset:52288
	ds_read_b64 v[190:191], v1 offset:52304
	ds_read_u16_d16_hi v220, v244 offset:11264
	ds_read_u16_d16_hi v221, v244 offset:11392
	ds_read_u16_d16_hi v222, v244 offset:11520
	ds_read_u16_d16_hi v223, v244 offset:11648
	ds_read_u16_d16_hi v224, v244 offset:12288
	ds_read_u16_d16_hi v225, v244 offset:12416
	ds_read_u16_d16_hi v226, v244 offset:12544
	ds_read_u16_d16_hi v227, v244 offset:12672
	v_mfma_f32_32x32x16_bf16 v[2:17], v[204:207], v[102:105], v[2:17]
	ds_read_b64 v[204:205], v1 offset:56896
	ds_read_b64 v[206:207], v1 offset:56912
	ds_read_u16_d16_hi v228, v244 offset:13312
	ds_read_u16_d16_hi v229, v244 offset:13440
	ds_read_u16_d16_hi v230, v244 offset:13568
	ds_read_u16_d16_hi v231, v244 offset:13696
	ds_read_u16_d16_hi v232, v244 offset:14336
	ds_read_u16_d16_hi v233, v244 offset:14464
	ds_read_u16_d16_hi v234, v244 offset:14592
	ds_read_u16_d16_hi v235, v244 offset:14720
	v_mfma_f32_32x32x16_bf16 v[18:33], v[192:195], v[98:101], v[18:33]
	ds_read_b64 v[192:193], v1 offset:52320
	ds_read_b64 v[194:195], v1 offset:52336
	ds_read_u16_d16_hi v236, v244 offset:15360
	ds_read_u16_d16_hi v237, v244 offset:15488
	ds_read_u16_d16_hi v238, v244 offset:15616
	ds_read_u16_d16_hi v239, v244 offset:15744
	ds_read_u16_d16_hi v240, v244 offset:16384
	ds_read_u16_d16_hi v241, v244 offset:16512
	ds_read_u16_d16_hi v242, v244 offset:16640
	ds_read_u16_d16_hi v243, v244 offset:16768
	v_mfma_f32_32x32x16_bf16 v[2:17], v[208:211], v[98:101], v[2:17]
	ds_read_b64 v[208:209], v1 offset:56928
	ds_read_b64 v[210:211], v1 offset:56944
	ds_write_b64 v187, v[110:111]
	ds_write_b64 v187, v[112:113] offset:16
	ds_write_b64 v187, v[106:107] offset:32
	ds_write_b64 v187, v[108:109] offset:48
	ds_write_b64 v187, v[102:103] offset:64
	ds_write_b64 v187, v[104:105] offset:80
	ds_write_b64 v187, v[98:99] offset:96
	ds_write_b64 v187, v[100:101] offset:112
	ds_read_b128 v[110:113], v247
	ds_read_b128 v[106:109], v247 offset:1152
	ds_read_b128 v[102:105], v247 offset:2304
	ds_read_b128 v[98:101], v247 offset:3456
	s_waitcnt lgkmcnt(0)
	global_store_dwordx4 v[248:249], v[110:113], off
	global_store_dwordx4 v[248:249], v[106:109], off offset:1024
	global_store_dwordx4 v[248:249], v[102:105], off offset:2048
	global_store_dwordx4 v[248:249], v[98:101], off offset:3072
	s_nop 1
	v_cvt_pk_bf16_f32 v110, v18, v19
	v_cvt_pk_bf16_f32 v111, v20, v21
	v_cvt_pk_bf16_f32 v112, v22, v23
	v_cvt_pk_bf16_f32 v113, v24, v25
	v_cvt_pk_bf16_f32 v106, v26, v27
	v_cvt_pk_bf16_f32 v107, v28, v29
	v_cvt_pk_bf16_f32 v108, v30, v31
	v_cvt_pk_bf16_f32 v109, v32, v33
	v_cvt_pk_bf16_f32 v102, v2, v3
	v_cvt_pk_bf16_f32 v103, v4, v5
	v_cvt_pk_bf16_f32 v104, v6, v7
	v_cvt_pk_bf16_f32 v105, v8, v9
	v_cvt_pk_bf16_f32 v98, v10, v11
	v_cvt_pk_bf16_f32 v99, v12, v13
	v_cvt_pk_bf16_f32 v100, v14, v15
	v_cvt_pk_bf16_f32 v101, v16, v17
	v_add_co_u32_e32 v248, vcc, s10, v148
	s_nop 1
	v_addc_co_u32_e32 v249, vcc, 0, v149, vcc
	s_waitcnt lgkmcnt(0)
	v_mfma_f32_32x32x16_bf16 v[18:33], v[178:181], v[110:113], v[212:227]
	ds_read_b64 v[178:179], v246 offset:0
	ds_read_b64 v[180:181], v246 offset:16
	v_mfma_f32_32x32x16_bf16 v[2:17], v[196:199], v[110:113], v[228:243]
	ds_read_b64 v[196:197], v246 offset:4608
	ds_read_b64 v[198:199], v246 offset:4624
	v_mfma_f32_32x32x16_bf16 v[18:33], v[182:185], v[106:109], v[18:33]
	ds_read_b64 v[182:183], v246 offset:32
	ds_read_b64 v[184:185], v246 offset:48
	v_mfma_f32_32x32x16_bf16 v[2:17], v[200:203], v[106:109], v[2:17]
	ds_read_b64 v[200:201], v246 offset:4640
	ds_read_b64 v[202:203], v246 offset:4656
	ds_read_u16_d16_hi v212, v244 offset:26624
	ds_read_u16_d16_hi v213, v244 offset:26752
	ds_read_u16_d16_hi v214, v244 offset:26880
	ds_read_u16_d16_hi v215, v244 offset:27008
	ds_read_u16_d16_hi v216, v244 offset:27648
	ds_read_u16_d16_hi v217, v244 offset:27776
	ds_read_u16_d16_hi v218, v244 offset:27904
	ds_read_u16_d16_hi v219, v244 offset:28032
	v_mfma_f32_32x32x16_bf16 v[18:33], v[188:191], v[102:105], v[18:33]
	ds_read_b64 v[188:189], v246 offset:64
	ds_read_b64 v[190:191], v246 offset:80
	ds_read_u16_d16_hi v220, v244 offset:28672
	ds_read_u16_d16_hi v221, v244 offset:28800
	ds_read_u16_d16_hi v222, v244 offset:28928
	ds_read_u16_d16_hi v223, v244 offset:29056
	ds_read_u16_d16_hi v224, v244 offset:29696
	ds_read_u16_d16_hi v225, v244 offset:29824
	ds_read_u16_d16_hi v226, v244 offset:29952
	ds_read_u16_d16_hi v227, v244 offset:30080
	v_mfma_f32_32x32x16_bf16 v[2:17], v[204:207], v[102:105], v[2:17]
	ds_read_b64 v[204:205], v246 offset:4672
	ds_read_b64 v[206:207], v246 offset:4688
	ds_read_u16_d16_hi v228, v244 offset:30720
	ds_read_u16_d16_hi v229, v244 offset:30848
	ds_read_u16_d16_hi v230, v244 offset:30976
	ds_read_u16_d16_hi v231, v244 offset:31104
	ds_read_u16_d16_hi v232, v244 offset:31744
	ds_read_u16_d16_hi v233, v244 offset:31872
	ds_read_u16_d16_hi v234, v244 offset:32000
	ds_read_u16_d16_hi v235, v244 offset:32128
	v_mfma_f32_32x32x16_bf16 v[18:33], v[192:195], v[98:101], v[18:33]
	ds_read_b64 v[192:193], v246 offset:96
	ds_read_b64 v[194:195], v246 offset:112
	ds_read_u16_d16_hi v236, v244 offset:32768
	ds_read_u16_d16_hi v237, v244 offset:32896
	ds_read_u16_d16_hi v238, v244 offset:33024
	ds_read_u16_d16_hi v239, v244 offset:33152
	ds_read_u16_d16_hi v240, v244 offset:33792
	ds_read_u16_d16_hi v241, v244 offset:33920
	ds_read_u16_d16_hi v242, v244 offset:34048
	ds_read_u16_d16_hi v243, v244 offset:34176
	v_mfma_f32_32x32x16_bf16 v[2:17], v[208:211], v[98:101], v[2:17]
	ds_read_b64 v[208:209], v246 offset:4704
	ds_read_b64 v[210:211], v246 offset:4720
	ds_write_b64 v187, v[110:111]
	ds_write_b64 v187, v[112:113] offset:16
	ds_write_b64 v187, v[106:107] offset:32
	ds_write_b64 v187, v[108:109] offset:48
	ds_write_b64 v187, v[102:103] offset:64
	ds_write_b64 v187, v[104:105] offset:80
	ds_write_b64 v187, v[98:99] offset:96
	ds_write_b64 v187, v[100:101] offset:112
	ds_read_b128 v[110:113], v247
	ds_read_b128 v[106:109], v247 offset:1152
	ds_read_b128 v[102:105], v247 offset:2304
	ds_read_b128 v[98:101], v247 offset:3456
	s_waitcnt lgkmcnt(0)
	global_store_dwordx4 v[248:249], v[110:113], off
	global_store_dwordx4 v[248:249], v[106:109], off offset:1024
	global_store_dwordx4 v[248:249], v[102:105], off offset:2048
	global_store_dwordx4 v[248:249], v[98:101], off offset:3072
	s_nop 1
	v_cvt_pk_bf16_f32 v110, v18, v19
	v_cvt_pk_bf16_f32 v111, v20, v21
	v_cvt_pk_bf16_f32 v112, v22, v23
	v_cvt_pk_bf16_f32 v113, v24, v25
	v_cvt_pk_bf16_f32 v106, v26, v27
	v_cvt_pk_bf16_f32 v107, v28, v29
	v_cvt_pk_bf16_f32 v108, v30, v31
	v_cvt_pk_bf16_f32 v109, v32, v33
	v_cvt_pk_bf16_f32 v102, v2, v3
	v_cvt_pk_bf16_f32 v103, v4, v5
	v_cvt_pk_bf16_f32 v104, v6, v7
	v_cvt_pk_bf16_f32 v105, v8, v9
	v_cvt_pk_bf16_f32 v98, v10, v11
	v_cvt_pk_bf16_f32 v99, v12, v13
	v_cvt_pk_bf16_f32 v100, v14, v15
	v_cvt_pk_bf16_f32 v101, v16, v17
	v_add_co_u32_e32 v248, vcc, s11, v148
	s_nop 1
	v_addc_co_u32_e32 v249, vcc, 0, v149, vcc
	s_waitcnt lgkmcnt(0)
	v_mfma_f32_32x32x16_bf16 v[18:33], v[178:181], v[110:113], v[212:227]
	ds_read_b64 v[178:179], v246 offset:17408
	ds_read_b64 v[180:181], v246 offset:17424
	v_mfma_f32_32x32x16_bf16 v[2:17], v[196:199], v[110:113], v[228:243]
	ds_read_b64 v[196:197], v246 offset:22016
	ds_read_b64 v[198:199], v246 offset:22032
	v_mfma_f32_32x32x16_bf16 v[18:33], v[182:185], v[106:109], v[18:33]
	ds_read_b64 v[182:183], v246 offset:17440
	ds_read_b64 v[184:185], v246 offset:17456
	v_mfma_f32_32x32x16_bf16 v[2:17], v[200:203], v[106:109], v[2:17]
	ds_read_b64 v[200:201], v246 offset:22048
	ds_read_b64 v[202:203], v246 offset:22064
	ds_read_u16_d16_hi v212, v244 offset:44032
	ds_read_u16_d16_hi v213, v244 offset:44160
	ds_read_u16_d16_hi v214, v244 offset:44288
	ds_read_u16_d16_hi v215, v244 offset:44416
	ds_read_u16_d16_hi v216, v244 offset:45056
	ds_read_u16_d16_hi v217, v244 offset:45184
	ds_read_u16_d16_hi v218, v244 offset:45312
	ds_read_u16_d16_hi v219, v244 offset:45440
	v_mfma_f32_32x32x16_bf16 v[18:33], v[188:191], v[102:105], v[18:33]
	ds_read_b64 v[188:189], v246 offset:17472
	ds_read_b64 v[190:191], v246 offset:17488
	ds_read_u16_d16_hi v220, v244 offset:46080
	ds_read_u16_d16_hi v221, v244 offset:46208
	ds_read_u16_d16_hi v222, v244 offset:46336
	ds_read_u16_d16_hi v223, v244 offset:46464
	ds_read_u16_d16_hi v224, v244 offset:47104
	ds_read_u16_d16_hi v225, v244 offset:47232
	ds_read_u16_d16_hi v226, v244 offset:47360
	ds_read_u16_d16_hi v227, v244 offset:47488
	v_mfma_f32_32x32x16_bf16 v[2:17], v[204:207], v[102:105], v[2:17]
	ds_read_b64 v[204:205], v246 offset:22080
	ds_read_b64 v[206:207], v246 offset:22096
	ds_read_u16_d16_hi v228, v244 offset:48128
	ds_read_u16_d16_hi v229, v244 offset:48256
	ds_read_u16_d16_hi v230, v244 offset:48384
	ds_read_u16_d16_hi v231, v244 offset:48512
	ds_read_u16_d16_hi v232, v244 offset:49152
	ds_read_u16_d16_hi v233, v244 offset:49280
	ds_read_u16_d16_hi v234, v244 offset:49408
	ds_read_u16_d16_hi v235, v244 offset:49536
	v_mfma_f32_32x32x16_bf16 v[18:33], v[192:195], v[98:101], v[18:33]
	ds_read_b64 v[192:193], v246 offset:17504
	ds_read_b64 v[194:195], v246 offset:17520
	ds_read_u16_d16_hi v236, v244 offset:50176
	ds_read_u16_d16_hi v237, v244 offset:50304
	ds_read_u16_d16_hi v238, v244 offset:50432
	ds_read_u16_d16_hi v239, v244 offset:50560
	ds_read_u16_d16_hi v240, v244 offset:51200
	ds_read_u16_d16_hi v241, v244 offset:51328
	ds_read_u16_d16_hi v242, v244 offset:51456
	ds_read_u16_d16_hi v243, v244 offset:51584
	v_mfma_f32_32x32x16_bf16 v[2:17], v[208:211], v[98:101], v[2:17]
	ds_read_b64 v[208:209], v246 offset:22112
	ds_read_b64 v[210:211], v246 offset:22128
	ds_write_b64 v187, v[110:111]
	ds_write_b64 v187, v[112:113] offset:16
	ds_write_b64 v187, v[106:107] offset:32
	ds_write_b64 v187, v[108:109] offset:48
	ds_write_b64 v187, v[102:103] offset:64
	ds_write_b64 v187, v[104:105] offset:80
	ds_write_b64 v187, v[98:99] offset:96
	ds_write_b64 v187, v[100:101] offset:112
	ds_read_b128 v[110:113], v247
	ds_read_b128 v[106:109], v247 offset:1152
	ds_read_b128 v[102:105], v247 offset:2304
	ds_read_b128 v[98:101], v247 offset:3456
	s_waitcnt lgkmcnt(0)
	global_store_dwordx4 v[248:249], v[110:113], off
	global_store_dwordx4 v[248:249], v[106:109], off offset:1024
	global_store_dwordx4 v[248:249], v[102:105], off offset:2048
	global_store_dwordx4 v[248:249], v[98:101], off offset:3072
	s_nop 1
	v_cvt_pk_bf16_f32 v110, v18, v19
	v_cvt_pk_bf16_f32 v111, v20, v21
	v_cvt_pk_bf16_f32 v112, v22, v23
	v_cvt_pk_bf16_f32 v113, v24, v25
	v_cvt_pk_bf16_f32 v106, v26, v27
	v_cvt_pk_bf16_f32 v107, v28, v29
	v_cvt_pk_bf16_f32 v108, v30, v31
	v_cvt_pk_bf16_f32 v109, v32, v33
	v_cvt_pk_bf16_f32 v102, v2, v3
	v_cvt_pk_bf16_f32 v103, v4, v5
	v_cvt_pk_bf16_f32 v104, v6, v7
	v_cvt_pk_bf16_f32 v105, v8, v9
	v_cvt_pk_bf16_f32 v98, v10, v11
	v_cvt_pk_bf16_f32 v99, v12, v13
	v_cvt_pk_bf16_f32 v100, v14, v15
	v_cvt_pk_bf16_f32 v101, v16, v17
	v_add_co_u32_e32 v248, vcc, s12, v148
	s_nop 1
	v_addc_co_u32_e32 v249, vcc, 0, v149, vcc
	s_waitcnt lgkmcnt(0)
	v_mfma_f32_32x32x16_bf16 v[18:33], v[178:181], v[110:113], v[212:227]
	ds_read_b64 v[178:179], v246 offset:34816
	ds_read_b64 v[180:181], v246 offset:34832
	v_mfma_f32_32x32x16_bf16 v[2:17], v[196:199], v[110:113], v[228:243]
	ds_read_b64 v[196:197], v246 offset:39424
	ds_read_b64 v[198:199], v246 offset:39440
	v_mfma_f32_32x32x16_bf16 v[18:33], v[182:185], v[106:109], v[18:33]
	ds_read_b64 v[182:183], v246 offset:34848
	ds_read_b64 v[184:185], v246 offset:34864
	v_mfma_f32_32x32x16_bf16 v[2:17], v[200:203], v[106:109], v[2:17]
	ds_read_b64 v[200:201], v246 offset:39456
	ds_read_b64 v[202:203], v246 offset:39472
	ds_read_u16_d16_hi v212, v245 offset:9216
	ds_read_u16_d16_hi v213, v245 offset:9344
	ds_read_u16_d16_hi v214, v245 offset:9472
	ds_read_u16_d16_hi v215, v245 offset:9600
	ds_read_u16_d16_hi v216, v245 offset:10240
	ds_read_u16_d16_hi v217, v245 offset:10368
	ds_read_u16_d16_hi v218, v245 offset:10496
	ds_read_u16_d16_hi v219, v245 offset:10624
	v_mfma_f32_32x32x16_bf16 v[18:33], v[188:191], v[102:105], v[18:33]
	ds_read_b64 v[188:189], v246 offset:34880
	ds_read_b64 v[190:191], v246 offset:34896
	ds_read_u16_d16_hi v220, v245 offset:11264
	ds_read_u16_d16_hi v221, v245 offset:11392
	ds_read_u16_d16_hi v222, v245 offset:11520
	ds_read_u16_d16_hi v223, v245 offset:11648
	ds_read_u16_d16_hi v224, v245 offset:12288
	ds_read_u16_d16_hi v225, v245 offset:12416
	ds_read_u16_d16_hi v226, v245 offset:12544
	ds_read_u16_d16_hi v227, v245 offset:12672
	v_mfma_f32_32x32x16_bf16 v[2:17], v[204:207], v[102:105], v[2:17]
	ds_read_b64 v[204:205], v246 offset:39488
	ds_read_b64 v[206:207], v246 offset:39504
	ds_read_u16_d16_hi v228, v245 offset:13312
	ds_read_u16_d16_hi v229, v245 offset:13440
	ds_read_u16_d16_hi v230, v245 offset:13568
	ds_read_u16_d16_hi v231, v245 offset:13696
	ds_read_u16_d16_hi v232, v245 offset:14336
	ds_read_u16_d16_hi v233, v245 offset:14464
	ds_read_u16_d16_hi v234, v245 offset:14592
	ds_read_u16_d16_hi v235, v245 offset:14720
	v_mfma_f32_32x32x16_bf16 v[18:33], v[192:195], v[98:101], v[18:33]
	ds_read_b64 v[192:193], v246 offset:34912
	ds_read_b64 v[194:195], v246 offset:34928
	ds_read_u16_d16_hi v236, v245 offset:15360
	ds_read_u16_d16_hi v237, v245 offset:15488
	ds_read_u16_d16_hi v238, v245 offset:15616
	ds_read_u16_d16_hi v239, v245 offset:15744
	ds_read_u16_d16_hi v240, v245 offset:16384
	ds_read_u16_d16_hi v241, v245 offset:16512
	ds_read_u16_d16_hi v242, v245 offset:16640
	ds_read_u16_d16_hi v243, v245 offset:16768
	v_mfma_f32_32x32x16_bf16 v[2:17], v[208:211], v[98:101], v[2:17]
	ds_read_b64 v[208:209], v246 offset:39520
	ds_read_b64 v[210:211], v246 offset:39536
	ds_write_b64 v187, v[110:111]
	ds_write_b64 v187, v[112:113] offset:16
	ds_write_b64 v187, v[106:107] offset:32
	ds_write_b64 v187, v[108:109] offset:48
	ds_write_b64 v187, v[102:103] offset:64
	ds_write_b64 v187, v[104:105] offset:80
	ds_write_b64 v187, v[98:99] offset:96
	ds_write_b64 v187, v[100:101] offset:112
	ds_read_b128 v[110:113], v247
	ds_read_b128 v[106:109], v247 offset:1152
	ds_read_b128 v[102:105], v247 offset:2304
	ds_read_b128 v[98:101], v247 offset:3456
	s_waitcnt lgkmcnt(0)
	global_store_dwordx4 v[248:249], v[110:113], off
	global_store_dwordx4 v[248:249], v[106:109], off offset:1024
	global_store_dwordx4 v[248:249], v[102:105], off offset:2048
	global_store_dwordx4 v[248:249], v[98:101], off offset:3072
	s_nop 1
	v_cvt_pk_bf16_f32 v110, v18, v19
	v_cvt_pk_bf16_f32 v111, v20, v21
	v_cvt_pk_bf16_f32 v112, v22, v23
	v_cvt_pk_bf16_f32 v113, v24, v25
	v_cvt_pk_bf16_f32 v106, v26, v27
	v_cvt_pk_bf16_f32 v107, v28, v29
	v_cvt_pk_bf16_f32 v108, v30, v31
	v_cvt_pk_bf16_f32 v109, v32, v33
	v_cvt_pk_bf16_f32 v102, v2, v3
	v_cvt_pk_bf16_f32 v103, v4, v5
	v_cvt_pk_bf16_f32 v104, v6, v7
	v_cvt_pk_bf16_f32 v105, v8, v9
	v_cvt_pk_bf16_f32 v98, v10, v11
	v_cvt_pk_bf16_f32 v99, v12, v13
	v_cvt_pk_bf16_f32 v100, v14, v15
	v_cvt_pk_bf16_f32 v101, v16, v17
	v_add_co_u32_e32 v248, vcc, s13, v148
	s_nop 1
	v_addc_co_u32_e32 v249, vcc, 0, v149, vcc
	s_waitcnt lgkmcnt(0)
	v_mfma_f32_32x32x16_bf16 v[18:33], v[178:181], v[110:113], v[212:227]
	ds_read_b64 v[178:179], v246 offset:52224
	ds_read_b64 v[180:181], v246 offset:52240
	v_mfma_f32_32x32x16_bf16 v[2:17], v[196:199], v[110:113], v[228:243]
	ds_read_b64 v[196:197], v246 offset:56832
	ds_read_b64 v[198:199], v246 offset:56848
	v_mfma_f32_32x32x16_bf16 v[18:33], v[182:185], v[106:109], v[18:33]
	ds_read_b64 v[182:183], v246 offset:52256
	ds_read_b64 v[184:185], v246 offset:52272
	v_mfma_f32_32x32x16_bf16 v[2:17], v[200:203], v[106:109], v[2:17]
	ds_read_b64 v[200:201], v246 offset:56864
	ds_read_b64 v[202:203], v246 offset:56880
	ds_read_u16_d16_hi v212, v245 offset:26624
	ds_read_u16_d16_hi v213, v245 offset:26752
	ds_read_u16_d16_hi v214, v245 offset:26880
	ds_read_u16_d16_hi v215, v245 offset:27008
	ds_read_u16_d16_hi v216, v245 offset:27648
	ds_read_u16_d16_hi v217, v245 offset:27776
	ds_read_u16_d16_hi v218, v245 offset:27904
	ds_read_u16_d16_hi v219, v245 offset:28032
	v_mfma_f32_32x32x16_bf16 v[18:33], v[188:191], v[102:105], v[18:33]
	ds_read_b64 v[188:189], v246 offset:52288
	ds_read_b64 v[190:191], v246 offset:52304
	ds_read_u16_d16_hi v220, v245 offset:28672
	ds_read_u16_d16_hi v221, v245 offset:28800
	ds_read_u16_d16_hi v222, v245 offset:28928
	ds_read_u16_d16_hi v223, v245 offset:29056
	ds_read_u16_d16_hi v224, v245 offset:29696
	ds_read_u16_d16_hi v225, v245 offset:29824
	ds_read_u16_d16_hi v226, v245 offset:29952
	ds_read_u16_d16_hi v227, v245 offset:30080
	v_mfma_f32_32x32x16_bf16 v[2:17], v[204:207], v[102:105], v[2:17]
	ds_read_b64 v[204:205], v246 offset:56896
	ds_read_b64 v[206:207], v246 offset:56912
	ds_read_u16_d16_hi v228, v245 offset:30720
	ds_read_u16_d16_hi v229, v245 offset:30848
	ds_read_u16_d16_hi v230, v245 offset:30976
	ds_read_u16_d16_hi v231, v245 offset:31104
	ds_read_u16_d16_hi v232, v245 offset:31744
	ds_read_u16_d16_hi v233, v245 offset:31872
	ds_read_u16_d16_hi v234, v245 offset:32000
	ds_read_u16_d16_hi v235, v245 offset:32128
	v_mfma_f32_32x32x16_bf16 v[18:33], v[192:195], v[98:101], v[18:33]
	ds_read_b64 v[192:193], v246 offset:52320
	ds_read_b64 v[194:195], v246 offset:52336
	ds_read_u16_d16_hi v236, v245 offset:32768
	ds_read_u16_d16_hi v237, v245 offset:32896
	ds_read_u16_d16_hi v238, v245 offset:33024
	ds_read_u16_d16_hi v239, v245 offset:33152
	ds_read_u16_d16_hi v240, v245 offset:33792
	ds_read_u16_d16_hi v241, v245 offset:33920
	ds_read_u16_d16_hi v242, v245 offset:34048
	ds_read_u16_d16_hi v243, v245 offset:34176
	v_mfma_f32_32x32x16_bf16 v[2:17], v[208:211], v[98:101], v[2:17]
	ds_read_b64 v[208:209], v246 offset:56928
	ds_read_b64 v[210:211], v246 offset:56944
	ds_write_b64 v187, v[110:111]
	ds_write_b64 v187, v[112:113] offset:16
	ds_write_b64 v187, v[106:107] offset:32
	ds_write_b64 v187, v[108:109] offset:48
	ds_write_b64 v187, v[102:103] offset:64
	ds_write_b64 v187, v[104:105] offset:80
	ds_write_b64 v187, v[98:99] offset:96
	ds_write_b64 v187, v[100:101] offset:112
	ds_read_b128 v[110:113], v247
	ds_read_b128 v[106:109], v247 offset:1152
	ds_read_b128 v[102:105], v247 offset:2304
	ds_read_b128 v[98:101], v247 offset:3456
	s_waitcnt lgkmcnt(0)
	global_store_dwordx4 v[248:249], v[110:113], off
	global_store_dwordx4 v[248:249], v[106:109], off offset:1024
	global_store_dwordx4 v[248:249], v[102:105], off offset:2048
	global_store_dwordx4 v[248:249], v[98:101], off offset:3072
	s_nop 1
	v_cvt_pk_bf16_f32 v110, v18, v19
	v_cvt_pk_bf16_f32 v111, v20, v21
	v_cvt_pk_bf16_f32 v112, v22, v23
	v_cvt_pk_bf16_f32 v113, v24, v25
	v_cvt_pk_bf16_f32 v106, v26, v27
	v_cvt_pk_bf16_f32 v107, v28, v29
	v_cvt_pk_bf16_f32 v108, v30, v31
	v_cvt_pk_bf16_f32 v109, v32, v33
	v_cvt_pk_bf16_f32 v102, v2, v3
	v_cvt_pk_bf16_f32 v103, v4, v5
	v_cvt_pk_bf16_f32 v104, v6, v7
	v_cvt_pk_bf16_f32 v105, v8, v9
	v_cvt_pk_bf16_f32 v98, v10, v11
	v_cvt_pk_bf16_f32 v99, v12, v13
	v_cvt_pk_bf16_f32 v100, v14, v15
	v_cvt_pk_bf16_f32 v101, v16, v17
	v_add_co_u32_e32 v248, vcc, s14, v148
	s_nop 1
	v_addc_co_u32_e32 v249, vcc, 0, v149, vcc
	s_waitcnt lgkmcnt(0)
	v_mfma_f32_32x32x16_bf16 v[18:33], v[178:181], v[110:113], v[212:227]
	v_mfma_f32_32x32x16_bf16 v[2:17], v[196:199], v[110:113], v[228:243]
	v_mfma_f32_32x32x16_bf16 v[18:33], v[182:185], v[106:109], v[18:33]
	v_mfma_f32_32x32x16_bf16 v[2:17], v[200:203], v[106:109], v[2:17]
	v_mfma_f32_32x32x16_bf16 v[18:33], v[188:191], v[102:105], v[18:33]
	v_mfma_f32_32x32x16_bf16 v[2:17], v[204:207], v[102:105], v[2:17]
	v_mfma_f32_32x32x16_bf16 v[18:33], v[192:195], v[98:101], v[18:33]
	v_mfma_f32_32x32x16_bf16 v[2:17], v[208:211], v[98:101], v[2:17]
	ds_write_b64 v187, v[110:111]
	ds_write_b64 v187, v[112:113] offset:16
	ds_write_b64 v187, v[106:107] offset:32
	ds_write_b64 v187, v[108:109] offset:48
	ds_write_b64 v187, v[102:103] offset:64
	ds_write_b64 v187, v[104:105] offset:80
	ds_write_b64 v187, v[98:99] offset:96
	ds_write_b64 v187, v[100:101] offset:112
	ds_read_b128 v[110:113], v247
	ds_read_b128 v[106:109], v247 offset:1152
	ds_read_b128 v[102:105], v247 offset:2304
	ds_read_b128 v[98:101], v247 offset:3456
	s_waitcnt lgkmcnt(0)
	global_store_dwordx4 v[248:249], v[110:113], off
	global_store_dwordx4 v[248:249], v[106:109], off offset:1024
	global_store_dwordx4 v[248:249], v[102:105], off offset:2048
	global_store_dwordx4 v[248:249], v[98:101], off offset:3072
	s_nop 1
	s_nop 4
	s_branch .LBB0_1922

	.amdhsa_kernel _ZN12_GLOBAL__N_14megaENS_4ArgsE
		.amdhsa_group_segment_fixed_size 9216
		.amdhsa_private_segment_fixed_size 0
		.amdhsa_kernarg_size 560
		.amdhsa_user_sgpr_count 2
		.amdhsa_user_sgpr_dispatch_ptr 0
		.amdhsa_user_sgpr_queue_ptr 0
		.amdhsa_user_sgpr_kernarg_segment_ptr 1
		.amdhsa_user_sgpr_dispatch_id 0
		.amdhsa_user_sgpr_kernarg_preload_length 0
		.amdhsa_user_sgpr_kernarg_preload_offset 0
		.amdhsa_user_sgpr_private_segment_size 0
		.amdhsa_uses_dynamic_stack 0
		.amdhsa_enable_private_segment 0
		.amdhsa_system_sgpr_workgroup_id_x 1
		.amdhsa_system_sgpr_workgroup_id_y 0
		.amdhsa_system_sgpr_workgroup_id_z 0
		.amdhsa_system_sgpr_workgroup_info 0
		.amdhsa_system_vgpr_workitem_id 0
		.amdhsa_next_free_vgpr 256
		.amdhsa_next_free_sgpr 98
		.amdhsa_accum_offset 256
		.amdhsa_reserve_vcc 1
		.amdhsa_float_round_mode_32 0
		.amdhsa_float_round_mode_16_64 0
		.amdhsa_float_denorm_mode_32 3
		.amdhsa_float_denorm_mode_16_64 3
		.amdhsa_dx10_clamp 1
		.amdhsa_ieee_mode 1
		.amdhsa_fp16_overflow 0
		.amdhsa_tg_split 0
		.amdhsa_exception_fp_ieee_invalid_op 0
		.amdhsa_exception_fp_denorm_src 0
		.amdhsa_exception_fp_ieee_div_zero 0
		.amdhsa_exception_fp_ieee_overflow 0
		.amdhsa_exception_fp_ieee_underflow 0
		.amdhsa_exception_fp_ieee_inexact 0
		.amdhsa_exception_int_div_zero 0
	.end_amdhsa_kernel

amdhsa.kernels:
  - .agpr_count:     0
    .args:
      - .offset:         0
        .size:           304
        .value_kind:     by_value
      - .offset:         304
        .size:           4
        .value_kind:     hidden_block_count_x
      - .offset:         308
        .size:           4
        .value_kind:     hidden_block_count_y
      - .offset:         312
        .size:           4
        .value_kind:     hidden_block_count_z
      - .offset:         316
        .size:           2
        .value_kind:     hidden_group_size_x
      - .offset:         318
        .size:           2
        .value_kind:     hidden_group_size_y
      - .offset:         320
        .size:           2
        .value_kind:     hidden_group_size_z
      - .offset:         322
        .size:           2
        .value_kind:     hidden_remainder_x
      - .offset:         324
        .size:           2
        .value_kind:     hidden_remainder_y
      - .offset:         326
        .size:           2
        .value_kind:     hidden_remainder_z
      - .offset:         344
        .size:           8
        .value_kind:     hidden_global_offset_x
      - .offset:         352
        .size:           8
        .value_kind:     hidden_global_offset_y
      - .offset:         360
        .size:           8
        .value_kind:     hidden_global_offset_z
      - .offset:         368
        .size:           2
        .value_kind:     hidden_grid_dims
      - .offset:         424
        .size:           4
        .value_kind:     hidden_dynamic_lds_size
    .group_segment_fixed_size: 9216
    .kernarg_segment_align: 8
    .kernarg_segment_size: 560
    .language:       OpenCL C
    .language_version:
      - 2
      - 0
    .max_flat_workgroup_size: 512
    .name:           _ZN12_GLOBAL__N_14megaENS_4ArgsE
    .private_segment_fixed_size: 0
    .sgpr_count:     104
    .sgpr_spill_count: 108
    .symbol:         _ZN12_GLOBAL__N_14megaENS_4ArgsE.kd
    .uniform_work_group_size: 1
    .uses_dynamic_stack: false
    .vgpr_count:     256
    .vgpr_spill_count: 0
    .wavefront_size: 64
